# expert-weight conversion queue: 2 items per claim (was 4 in the previous version, 8 in the baseline)
# baseline (speedup 1.0000x reference)
; #define RI_NEXT(D_) do { if (q.cnt == 8) { int b_ = 0; if (F.lane == 0) b_ = (int)__hip_atomic_fetch_add(qctr, 8u, __ATOMIC_RELAXED, __HIP_MEMORY_SCOPE_AGENT); q.base = __builtin_amdgcn_readfirstlane(b_); q.cnt = 0; } \
;         D_ = decode_item(KA, F.ws, kind, q.base + q.cnt); ++q.cnt; } while (0)
; DI void run_items1(Frame& F, int kind, int quota, QState& q) {
;     ...
;     if (quota == 0) return;
;     TItem d; RI_NEXT(d); if (!d.valid) return;
; DI void phase_attn(Frame& F, int l) {
;     ...
;     QState cq; cq.base = 0; cq.cnt = 8;
;     constexpr int SLOT_ITEMS = 3;
;     if (F.bid & 1) { __syncthreads(); run_items1(F, 1 + l, SLOT_ITEMS, cq); }
.LBB0_398:
	v_readlane_b32 s8, v255, 14
	v_readlane_b32 s4, v253, 8
	s_lshl_b32 s58, s8, 6
	v_readlane_b32 s6, v253, 10
	v_readlane_b32 s7, v253, 11
	s_lshl_b64 s[0:1], s[58:59], 2
	s_mov_b64 s[2:3], s[6:7]
	s_add_u32 s0, s2, s0
	s_addc_u32 s1, s3, s1
	v_readlane_b32 s9, v255, 15
	s_add_u32 s12, s0, 0x8100
	s_addc_u32 s13, s1, 0
	s_lshl_b64 s[0:1], s[8:9], 25
	v_writelane_b32 v255, s0, 16
	s_lshl_b64 s[62:63], s[8:9], 5
	s_lshl_b32 s2, s8, 20
	v_writelane_b32 v255, s1, 17
	s_mov_b32 s3, s59
	v_readlane_b32 s0, v253, 33
	v_writelane_b32 v255, s2, 18
	s_add_u32 s76, s0, s2
	v_readlane_b32 s0, v253, 34
	v_writelane_b32 v255, s3, 19
	s_addc_u32 s77, s0, 0
	s_lshl_b64 s[20:21], s[8:9], 21
	s_lshl_b64 s[0:1], s[8:9], 20
	v_readlane_b32 s2, v253, 35
	s_add_u32 s22, s2, s0
	v_readlane_b32 s2, v253, 36
	s_addc_u32 s23, s2, s1
	v_readlane_b32 s2, v253, 37
	s_add_u32 s24, s2, s0
	v_readlane_b32 s0, v253, 38
	s_addc_u32 s25, s0, s1
	s_lshl_b64 s[26:27], s[8:9], 24
	v_readlane_b32 s0, v253, 39
	s_add_u32 s14, s0, s44
	v_readlane_b32 s0, v253, 40
	s_addc_u32 s15, s0, s45
	s_mov_b32 s0, -1
	s_mov_b32 s95, 0
	v_mbcnt_lo_u32_b32 v0, s0, 0
	v_mbcnt_hi_u32_b32 v186, s0, v0
	v_readlane_b32 s0, v253, 29
	s_mov_b32 s51, s0
	s_mov_b64 s[30:31], s[70:71]
	s_bitcmp0_b32 s51, 0
	s_mov_b32 s63, 2
	v_readlane_b32 s5, v253, 9
	v_readlane_b32 s1, v253, 30
	s_cbranch_scc1 .LBB0_472
	s_mov_b64 s[6:7], s[70:71]
	v_mov_b32_e32 v0, 0
	v_cmp_eq_u32_e64 s[4:5], 0, v186
	s_waitcnt vmcnt(63) expcnt(7) lgkmcnt(15)
	s_barrier
	s_and_saveexec_b64 s[2:3], s[4:5]
	s_cbranch_execz .LBB0_403
	s_mov_b64 s[10:11], exec
	v_mbcnt_lo_u32_b32 v0, s10, 0
	v_mbcnt_hi_u32_b32 v0, s11, v0
	v_cmp_eq_u32_e32 vcc, 0, v0
	s_and_saveexec_b64 s[8:9], vcc
	s_cbranch_execz .LBB0_402
	s_bcnt1_i32_b64 s0, s[10:11]
	s_lshl_b32 s0, s0, 1
	v_mov_b32_e32 v2, s0
	global_atomic_add v2, v1, v2, s[12:13] sc0
.LBB0_402:
	s_or_b64 exec, exec, s[8:9]
	s_waitcnt vmcnt(0)
	v_readfirstlane_b32 s0, v2
	s_nop 1
	v_lshl_add_u32 v0, v0, 1, s0

; #define LDS_WAIT() asm volatile("s_waitcnt lgkmcnt(0)" ::: "memory")
; #define RI_NEXT(D_) do { if (q.cnt == 8) { int b_ = 0; if (F.lane == 0) b_ = (int)__hip_atomic_fetch_add(qctr, 8u, __ATOMIC_RELAXED, __HIP_MEMORY_SCOPE_AGENT); q.base = __builtin_amdgcn_readfirstlane(b_); q.cnt = 0; } \
;         D_ = decode_item(KA, F.ws, kind, q.base + q.cnt); ++q.cnt; } while (0)
; DI void item_scatter(const f32x4 (&v)[16], LAS float* scr, int lane) {
;     ...
;     for (int i = 0; i < 16; ++i) { const int k = 4 * i + r4;
; #pragma unroll
;         for (int j = 0; j < 4; ++j) scr[(4 * c4 + j) * 64 + (k ^ (4 * (c4 ^ j)))] = v[i][j]; }
;     LDS_WAIT(); asm volatile("" ::: "memory");
; DI void run_items1(Frame& F, int kind, int quota, QState& q) {
;     ...
;         item_scatter(v, scr, F.lane);
;         TItem dn; dn.valid = false;
;         if (quota < 0 || n < quota) { RI_NEXT(dn); if (dn.valid) item_load(dn, v, F.lane); }
.LBB0_430:
	s_waitcnt vmcnt(0)
	ds_write_b32 v93, v2
	ds_write_b32 v94, v3 offset:256
	ds_write_b32 v95, v4 offset:512
	ds_write_b32 v96, v5 offset:768
	ds_write_b32 v97, v6
	ds_write_b32 v98, v7 offset:256
	ds_write_b32 v99, v8 offset:512
	ds_write_b32 v100, v9 offset:768
	ds_write_b32 v101, v10
	ds_write_b32 v102, v11 offset:256
	ds_write_b32 v103, v12 offset:512
	ds_write_b32 v104, v13 offset:768
	ds_write_b32 v105, v14
	ds_write_b32 v106, v15 offset:256
	ds_write_b32 v107, v16 offset:512
	ds_write_b32 v108, v17 offset:768
	ds_write_b32 v109, v18
	ds_write_b32 v110, v19 offset:256
	ds_write_b32 v111, v20 offset:512
	ds_write_b32 v112, v21 offset:768
	ds_write_b32 v113, v22
	ds_write_b32 v114, v23 offset:256
	ds_write_b32 v115, v24 offset:512
	ds_write_b32 v116, v25 offset:768
	ds_write_b32 v117, v26
	ds_write_b32 v118, v27 offset:256
	ds_write_b32 v119, v28 offset:512
	ds_write_b32 v120, v29 offset:768
	ds_write_b32 v121, v30
	ds_write_b32 v122, v31 offset:256
	ds_write_b32 v123, v32 offset:512
	ds_write_b32 v124, v33 offset:768
	ds_write_b32 v125, v34
	ds_write_b32 v126, v35 offset:256
	ds_write_b32 v127, v36 offset:512
	ds_write_b32 v128, v37 offset:768
	ds_write_b32 v129, v38
	ds_write_b32 v130, v39 offset:256
	ds_write_b32 v131, v40 offset:512
	ds_write_b32 v132, v41 offset:768
	ds_write_b32 v133, v42
	ds_write_b32 v134, v43 offset:256
	ds_write_b32 v135, v44 offset:512
	ds_write_b32 v136, v45 offset:768
	ds_write_b32 v137, v46
	ds_write_b32 v138, v47 offset:256
	ds_write_b32 v139, v48 offset:512
	ds_write_b32 v140, v49 offset:768
	ds_write_b32 v141, v50
	ds_write_b32 v142, v51 offset:256
	ds_write_b32 v143, v52 offset:512
	ds_write_b32 v144, v53 offset:768
	ds_write_b32 v145, v54
	ds_write_b32 v146, v55 offset:256
	ds_write_b32 v147, v56 offset:512
	ds_write_b32 v148, v57 offset:768
	ds_write_b32 v149, v58
	ds_write_b32 v150, v59 offset:256
	ds_write_b32 v151, v60 offset:512
	ds_write_b32 v152, v61 offset:768
	ds_write_b32 v153, v62
	ds_write_b32 v154, v63 offset:256
	ds_write_b32 v155, v64 offset:512
	ds_write_b32 v156, v65 offset:768
	s_waitcnt lgkmcnt(0)
	s_cmp_gt_u32 s38, 2
	s_mov_b64 s[2:3], 0
	s_cbranch_scc1 .LBB0_465
	s_cmp_lg_u32 s63, 2
	s_cbranch_scc1 .LBB0_437
	v_mov_b32_e32 v0, 0
	s_and_saveexec_b64 s[2:3], s[4:5]
	s_cbranch_execz .LBB0_436
	s_mov_b64 s[18:19], exec
	v_mbcnt_lo_u32_b32 v0, s18, 0
	v_mbcnt_hi_u32_b32 v0, s19, v0
	v_cmp_eq_u32_e32 vcc, 0, v0
	s_and_saveexec_b64 s[16:17], vcc
	s_cbranch_execz .LBB0_435
	s_bcnt1_i32_b64 s0, s[18:19]
	s_lshl_b32 s0, s0, 1
	v_mov_b32_e32 v66, s0
	global_atomic_add v66, v1, v66, s[12:13] sc0
.LBB0_435:
	s_or_b64 exec, exec, s[16:17]
	s_waitcnt vmcnt(0)
	v_readfirstlane_b32 s0, v66
	s_nop 1
	v_lshl_add_u32 v0, v0, 1, s0

; DI unsigned pk4_fp8(float a, float b, float c, float d) { int r = 0; r = __builtin_amdgcn_cvt_pk_fp8_f32(sat8(a), sat8(b), r, false); r = __builtin_amdgcn_cvt_pk_fp8_f32(sat8(c), sat8(d), r, true); return (unsigned)r; }
; DI float half_sum(float v) { const auto rr = __builtin_amdgcn_permlane32_swap(__float_as_uint(v), __float_as_uint(v), false, false); return __uint_as_float(rr[0]) + __uint_as_float(rr[1]); }
; DI void phase_attn(Frame& F, int l) {
;     ...
;         const float ltot = half_sum(l_run); const float inv = AZ8_SCALE / ltot;
; #pragma unroll
;         for (int ds = 0; ds < 2; ++ds)
; #pragma unroll
;             for (int g4 = 0; g4 < 4; g4 += 2) {
;                 const unsigned wa = pk4_fp8(o[ds][4 * g4] * inv, o[ds][4 * g4 + 1] * inv, o[ds][4 * g4 + 2] * inv, o[ds][4 * g4 + 3] * inv), wb = pk4_fp8(o[ds][4 * g4 + 4] * inv, o[ds][4 * g4 + 5] * inv, o[ds][4 * g4 + 6] * inv, o[ds][4 * g4 + 7] * inv);
;                 const auto rr = __builtin_amdgcn_permlane32_swap(wa, wb, false, false);
;                 u32x2 w; w.x = rr[0]; w.y = rr[1];
;                 *(u32x2*)(att + qtok * D + h * HD + 32 * ds + 8 * (g4 + hh)) = w; }
;         if (!((F.bid & 1) && it == 3)) { __syncthreads(); run_items1(F, 1 + l, SLOT_ITEMS, cq); }
.LBB0_568:
	v_mov_b32_e32 v0, v11
	s_nop 1
	v_permlane32_swap_b32_e32 v11, v0
	v_add_f32_e32 v0, v11, v0
	s_mov_b32 s2, 0x41000000
	s_waitcnt vmcnt(1)
	v_div_scale_f32 v2, s[0:1], v0, v0, s2
	v_rcp_f32_e32 v3, v2
	v_readlane_b32 s0, v253, 21
	v_readlane_b32 s1, v253, 22
	s_bitcmp1_b32 s19, 0
	v_fma_f32 v4, -v2, v3, 1.0
	v_fmac_f32_e32 v3, v4, v3
	v_div_scale_f32 v4, vcc, s2, v0, s2
	v_mul_f32_e32 v5, v4, v3
	s_waitcnt vmcnt(0)
	v_fma_f32 v6, -v2, v5, v4
	v_fmac_f32_e32 v5, v6, v3
	v_fma_f32 v2, -v2, v5, v4
	v_div_fmas_f32 v2, v2, v3, v5
	v_div_fixup_f32 v0, v2, v0, s2
	v_mul_f32_e32 v2, v16, v0
	v_mul_f32_e32 v3, v17, v0
	v_med3_f32 v5, v2, s53, v204
	v_med3_f32 v3, v3, s53, v204
	v_mov_b32_e32 v2, v1
	v_cvt_pk_fp8_f32 v2, v5, v3
	v_mul_f32_e32 v4, v18, v0
	v_mul_f32_e32 v3, v19, v0
	v_med3_f32 v4, v4, s53, v204
	v_med3_f32 v3, v3, s53, v204
	v_cvt_pk_fp8_f32 v2, v4, v3 op_sel:[0,0,1]
	v_mul_f32_e32 v3, v20, v0
	v_mul_f32_e32 v4, v21, v0
	v_med3_f32 v6, v3, s53, v204
	v_med3_f32 v4, v4, s53, v204
	v_mov_b32_e32 v3, v1
	v_cvt_pk_fp8_f32 v3, v6, v4
	v_mul_f32_e32 v6, v24, v0
	v_mul_f32_e32 v7, v25, v0
	v_med3_f32 v9, v6, s53, v204
	v_med3_f32 v7, v7, s53, v204
	v_mov_b32_e32 v6, v1
	v_cvt_pk_fp8_f32 v6, v9, v7
	v_mul_f32_e32 v8, v26, v0
	v_mul_f32_e32 v7, v27, v0
	v_med3_f32 v8, v8, s53, v204
	v_med3_f32 v7, v7, s53, v204
	v_cvt_pk_fp8_f32 v6, v8, v7 op_sel:[0,0,1]
	v_mul_f32_e32 v7, v28, v0
	v_mul_f32_e32 v8, v29, v0
	v_med3_f32 v10, v7, s53, v204
	v_med3_f32 v8, v8, s53, v204
	v_mov_b32_e32 v7, v1
	v_cvt_pk_fp8_f32 v7, v10, v8
	v_mul_f32_e32 v5, v22, v0
	v_mul_f32_e32 v4, v23, v0
	v_med3_f32 v5, v5, s53, v204
	v_med3_f32 v4, v4, s53, v204
	v_mul_f32_e32 v9, v30, v0
	v_mul_f32_e32 v8, v31, v0
	v_cvt_pk_fp8_f32 v3, v5, v4 op_sel:[0,0,1]
	v_med3_f32 v9, v9, s53, v204
	v_med3_f32 v8, v8, s53, v204
	v_cvt_pk_fp8_f32 v7, v9, v8 op_sel:[0,0,1]
	v_lshl_add_u64 v[4:5], s[0:1], 0, v[170:171]
	v_lshl_add_u64 v[4:5], v[4:5], 0, s[58:59]
	v_permlane32_swap_b32_e32 v2, v3
	v_lshl_add_u64 v[4:5], v[4:5], 0, v[168:169]
	global_store_dwordx2 v[4:5], v[2:3], off
	v_permlane32_swap_b32_e32 v6, v7
	v_mul_f32_e32 v2, v32, v0
	v_mul_f32_e32 v3, v33, v0
	global_store_dwordx2 v[4:5], v[6:7], off offset:16
	v_med3_f32 v7, v2, s53, v204
	v_med3_f32 v3, v3, s53, v204
	v_mov_b32_e32 v2, v1
	v_cvt_pk_fp8_f32 v2, v7, v3
	v_mul_f32_e32 v6, v34, v0
	v_mul_f32_e32 v3, v35, v0
	v_med3_f32 v6, v6, s53, v204
	v_med3_f32 v3, v3, s53, v204
	v_cvt_pk_fp8_f32 v2, v6, v3 op_sel:[0,0,1]
	v_mul_f32_e32 v3, v36, v0
	v_mul_f32_e32 v6, v37, v0
	v_med3_f32 v8, v3, s53, v204
	v_med3_f32 v6, v6, s53, v204
	v_mov_b32_e32 v3, v1
	v_cvt_pk_fp8_f32 v3, v8, v6
	v_mul_f32_e32 v7, v38, v0
	v_mul_f32_e32 v6, v39, v0
	v_med3_f32 v7, v7, s53, v204
	v_med3_f32 v6, v6, s53, v204
	v_cvt_pk_fp8_f32 v3, v7, v6 op_sel:[0,0,1]
	v_mul_f32_e32 v6, v40, v0
	v_mul_f32_e32 v7, v41, v0
	v_med3_f32 v9, v6, s53, v204
	v_med3_f32 v7, v7, s53, v204
	v_mov_b32_e32 v6, v1
	v_cvt_pk_fp8_f32 v6, v9, v7
	v_mul_f32_e32 v8, v42, v0
	v_mul_f32_e32 v7, v43, v0
	v_med3_f32 v8, v8, s53, v204
	v_med3_f32 v7, v7, s53, v204
	v_cvt_pk_fp8_f32 v6, v8, v7 op_sel:[0,0,1]
	v_mul_f32_e32 v7, v44, v0
	v_mul_f32_e32 v8, v45, v0
	v_med3_f32 v10, v7, s53, v204
	v_med3_f32 v8, v8, s53, v204
	v_mov_b32_e32 v7, v1
	v_cvt_pk_fp8_f32 v7, v10, v8
	v_mul_f32_e32 v9, v46, v0
	v_mul_f32_e32 v0, v47, v0
	v_med3_f32 v8, v9, s53, v204
	v_med3_f32 v0, v0, s53, v204
	v_cvt_pk_fp8_f32 v7, v8, v0 op_sel:[0,0,1]
	s_cselect_b64 s[0:1], -1, 0
	s_cmp_eq_u32 s18, 3
	s_cselect_b64 s[2:3], -1, 0
	s_and_b64 s[0:1], s[2:3], s[0:1]
	v_permlane32_swap_b32_e32 v2, v3
	v_permlane32_swap_b32_e32 v6, v7
	s_and_b64 vcc, exec, s[0:1]
	global_store_dwordx2 v[4:5], v[2:3], off offset:32
	global_store_dwordx2 v[4:5], v[6:7], off offset:48
	s_cbranch_vccnz .LBB0_474
	s_mov_b64 s[6:7], s[70:71]
	s_cmp_lg_u32 s63, 2
	s_barrier
	s_cbranch_scc1 .LBB0_575
	v_mov_b32_e32 v0, 0
	s_and_saveexec_b64 s[2:3], s[4:5]
	s_cbranch_execz .LBB0_574
	s_mov_b64 s[10:11], exec
	v_mbcnt_lo_u32_b32 v0, s10, 0
	v_mbcnt_hi_u32_b32 v0, s11, v0
	v_cmp_eq_u32_e32 vcc, 0, v0
	s_and_saveexec_b64 s[8:9], vcc
	s_cbranch_execz .LBB0_573
	s_bcnt1_i32_b64 s0, s[10:11]
	s_lshl_b32 s0, s0, 1
	v_mov_b32_e32 v2, s0
	global_atomic_add v2, v1, v2, s[12:13] sc0

; #define LDS_WAIT() asm volatile("s_waitcnt lgkmcnt(0)" ::: "memory")
; #define RI_NEXT(D_) do { if (q.cnt == 8) { int b_ = 0; if (F.lane == 0) b_ = (int)__hip_atomic_fetch_add(qctr, 8u, __ATOMIC_RELAXED, __HIP_MEMORY_SCOPE_AGENT); q.base = __builtin_amdgcn_readfirstlane(b_); q.cnt = 0; } \
;         D_ = decode_item(KA, F.ws, kind, q.base + q.cnt); ++q.cnt; } while (0)
; DI void item_scatter(const f32x4 (&v)[16], LAS float* scr, int lane) {
;     ...
;     for (int i = 0; i < 16; ++i) { const int k = 4 * i + r4;
; #pragma unroll
;         for (int j = 0; j < 4; ++j) scr[(4 * c4 + j) * 64 + (k ^ (4 * (c4 ^ j)))] = v[i][j]; }
;     LDS_WAIT(); asm volatile("" ::: "memory");
; DI void run_items1(Frame& F, int kind, int quota, QState& q) {
;     ...
;         item_scatter(v, scr, F.lane);
;         TItem dn; dn.valid = false;
;         if (quota < 0 || n < quota) { RI_NEXT(dn); if (dn.valid) item_load(dn, v, F.lane); }
.LBB0_602:
	s_waitcnt vmcnt(15)
	ds_write_b32 v93, v2
	ds_write_b32 v94, v3 offset:256
	ds_write_b32 v95, v4 offset:512
	ds_write_b32 v96, v5 offset:768
	s_waitcnt vmcnt(14)
	ds_write_b32 v97, v6
	ds_write_b32 v98, v7 offset:256
	ds_write_b32 v99, v8 offset:512
	ds_write_b32 v100, v9 offset:768
	s_waitcnt vmcnt(13)
	ds_write_b32 v101, v10
	ds_write_b32 v102, v11 offset:256
	ds_write_b32 v103, v12 offset:512
	ds_write_b32 v104, v13 offset:768
	s_waitcnt vmcnt(12)
	ds_write_b32 v105, v14
	ds_write_b32 v106, v15 offset:256
	ds_write_b32 v107, v16 offset:512
	ds_write_b32 v108, v17 offset:768
	s_waitcnt vmcnt(11)
	ds_write_b32 v109, v18
	ds_write_b32 v110, v19 offset:256
	ds_write_b32 v111, v20 offset:512
	ds_write_b32 v112, v21 offset:768
	s_waitcnt vmcnt(10)
	ds_write_b32 v113, v22
	ds_write_b32 v114, v23 offset:256
	ds_write_b32 v115, v24 offset:512
	ds_write_b32 v116, v25 offset:768
	s_waitcnt vmcnt(9)
	ds_write_b32 v117, v26
	ds_write_b32 v118, v27 offset:256
	ds_write_b32 v119, v28 offset:512
	ds_write_b32 v120, v29 offset:768
	s_waitcnt vmcnt(8)
	ds_write_b32 v121, v30
	ds_write_b32 v122, v31 offset:256
	ds_write_b32 v123, v32 offset:512
	ds_write_b32 v124, v33 offset:768
	s_waitcnt vmcnt(7)
	ds_write_b32 v125, v34
	ds_write_b32 v126, v35 offset:256
	ds_write_b32 v127, v36 offset:512
	ds_write_b32 v128, v37 offset:768
	s_waitcnt vmcnt(6)
	ds_write_b32 v129, v38
	ds_write_b32 v130, v39 offset:256
	ds_write_b32 v131, v40 offset:512
	ds_write_b32 v132, v41 offset:768
	s_waitcnt vmcnt(5)
	ds_write_b32 v133, v42
	ds_write_b32 v134, v43 offset:256
	ds_write_b32 v135, v44 offset:512
	ds_write_b32 v136, v45 offset:768
	s_waitcnt vmcnt(4)
	ds_write_b32 v137, v46
	ds_write_b32 v138, v47 offset:256
	ds_write_b32 v139, v48 offset:512
	ds_write_b32 v140, v49 offset:768
	s_waitcnt vmcnt(3)
	ds_write_b32 v141, v50
	ds_write_b32 v142, v51 offset:256
	ds_write_b32 v143, v52 offset:512
	ds_write_b32 v144, v53 offset:768
	s_waitcnt vmcnt(2)
	ds_write_b32 v145, v54
	ds_write_b32 v146, v55 offset:256
	ds_write_b32 v147, v56 offset:512
	ds_write_b32 v148, v57 offset:768
	s_waitcnt vmcnt(1)
	ds_write_b32 v149, v58
	ds_write_b32 v150, v59 offset:256
	ds_write_b32 v151, v60 offset:512
	ds_write_b32 v152, v61 offset:768
	s_waitcnt vmcnt(0)
	ds_write_b32 v153, v62
	ds_write_b32 v154, v63 offset:256
	ds_write_b32 v155, v64 offset:512
	ds_write_b32 v156, v65 offset:768
	s_waitcnt lgkmcnt(0)
	s_cmp_gt_u32 s38, 2
	s_mov_b64 s[2:3], 0
	s_cbranch_scc1 .LBB0_637
	s_cmp_lg_u32 s63, 2
	s_cbranch_scc1 .LBB0_609
	v_mov_b32_e32 v0, 0
	s_and_saveexec_b64 s[2:3], s[4:5]
	s_cbranch_execz .LBB0_608
	s_mov_b64 s[18:19], exec
	v_mbcnt_lo_u32_b32 v0, s18, 0
	v_mbcnt_hi_u32_b32 v0, s19, v0
	v_cmp_eq_u32_e32 vcc, 0, v0
	s_and_saveexec_b64 s[16:17], vcc
	s_cbranch_execz .LBB0_607
	s_bcnt1_i32_b64 s0, s[18:19]
	s_lshl_b32 s0, s0, 1
	v_mov_b32_e32 v66, s0
	global_atomic_add v66, v1, v66, s[12:13] sc0

; DI void phase_attn(Frame& F, int l) {
;     ...
;     __syncthreads();
;     run_items1(F, 1 + l, -1, cq);
.LBB0_645:
	s_mov_b64 s[6:7], s[70:71]
	s_cmp_lg_u32 s63, 2
	s_waitcnt lgkmcnt(0)
	s_barrier
	s_cbranch_scc1 .LBB0_651
	v_mov_b32_e32 v0, 0
	v_cmp_eq_u32_e32 vcc, 0, v186
	s_and_saveexec_b64 s[2:3], vcc
	s_cbranch_execz .LBB0_650
	s_mov_b64 s[8:9], exec
	v_mbcnt_lo_u32_b32 v0, s8, 0
	v_mbcnt_hi_u32_b32 v0, s9, v0
	v_cmp_eq_u32_e32 vcc, 0, v0
	s_and_saveexec_b64 s[4:5], vcc
	s_cbranch_execz .LBB0_649
	s_bcnt1_i32_b64 s0, s[8:9]
	s_lshl_b32 s0, s0, 1
	s_waitcnt vmcnt(0)
	v_mov_b32_e32 v2, s0
	global_atomic_add v2, v1, v2, s[12:13] sc0
.LBB0_649:
	s_or_b64 exec, exec, s[4:5]
	s_waitcnt vmcnt(0)
	v_readfirstlane_b32 s0, v2
	s_nop 1
	v_lshl_add_u32 v0, v0, 1, s0

; #define LDS_WAIT() asm volatile("s_waitcnt lgkmcnt(0)" ::: "memory")
; #define RI_NEXT(D_) do { if (q.cnt == 8) { int b_ = 0; if (F.lane == 0) b_ = (int)__hip_atomic_fetch_add(qctr, 8u, __ATOMIC_RELAXED, __HIP_MEMORY_SCOPE_AGENT); q.base = __builtin_amdgcn_readfirstlane(b_); q.cnt = 0; } \
;         D_ = decode_item(KA, F.ws, kind, q.base + q.cnt); ++q.cnt; } while (0)
; DI void item_scatter(const f32x4 (&v)[16], LAS float* scr, int lane) {
;     ...
;     for (int i = 0; i < 16; ++i) { const int k = 4 * i + r4;
; #pragma unroll
;         for (int j = 0; j < 4; ++j) scr[(4 * c4 + j) * 64 + (k ^ (4 * (c4 ^ j)))] = v[i][j]; }
;     LDS_WAIT(); asm volatile("" ::: "memory");
; DI void run_items1(Frame& F, int kind, int quota, QState& q) {
;     ...
;     for (int n = 1; ; ++n) {
;         item_scatter(v, scr, F.lane);
;         TItem dn; dn.valid = false;
;         if (quota < 0 || n < quota) { RI_NEXT(dn); if (dn.valid) item_load(dn, v, F.lane); }
.LBB0_678:
	s_waitcnt vmcnt(15)
	ds_write_b32 v93, v2
	ds_write_b32 v94, v3 offset:256
	ds_write_b32 v95, v4 offset:512
	ds_write_b32 v96, v5 offset:768
	s_waitcnt vmcnt(14)
	ds_write_b32 v97, v6
	ds_write_b32 v98, v7 offset:256
	ds_write_b32 v99, v8 offset:512
	ds_write_b32 v100, v9 offset:768
	s_waitcnt vmcnt(13)
	ds_write_b32 v101, v10
	ds_write_b32 v102, v11 offset:256
	ds_write_b32 v103, v12 offset:512
	ds_write_b32 v104, v13 offset:768
	s_waitcnt vmcnt(12)
	ds_write_b32 v105, v14
	ds_write_b32 v106, v15 offset:256
	ds_write_b32 v107, v16 offset:512
	ds_write_b32 v108, v17 offset:768
	s_waitcnt vmcnt(11)
	ds_write_b32 v109, v18
	ds_write_b32 v110, v19 offset:256
	ds_write_b32 v111, v20 offset:512
	ds_write_b32 v112, v21 offset:768
	s_waitcnt vmcnt(10)
	ds_write_b32 v113, v22
	ds_write_b32 v114, v23 offset:256
	ds_write_b32 v115, v24 offset:512
	ds_write_b32 v116, v25 offset:768
	s_waitcnt vmcnt(9)
	ds_write_b32 v117, v26
	ds_write_b32 v118, v27 offset:256
	ds_write_b32 v119, v28 offset:512
	ds_write_b32 v120, v29 offset:768
	s_waitcnt vmcnt(8)
	ds_write_b32 v121, v30
	ds_write_b32 v122, v31 offset:256
	ds_write_b32 v123, v32 offset:512
	ds_write_b32 v124, v33 offset:768
	s_waitcnt vmcnt(7)
	ds_write_b32 v125, v34
	ds_write_b32 v126, v35 offset:256
	ds_write_b32 v127, v36 offset:512
	ds_write_b32 v128, v37 offset:768
	s_waitcnt vmcnt(6)
	ds_write_b32 v129, v38
	ds_write_b32 v130, v39 offset:256
	ds_write_b32 v131, v40 offset:512
	ds_write_b32 v132, v41 offset:768
	s_waitcnt vmcnt(5)
	ds_write_b32 v133, v42
	ds_write_b32 v134, v43 offset:256
	ds_write_b32 v135, v44 offset:512
	ds_write_b32 v136, v45 offset:768
	s_waitcnt vmcnt(4)
	ds_write_b32 v137, v46
	ds_write_b32 v138, v47 offset:256
	ds_write_b32 v139, v48 offset:512
	ds_write_b32 v140, v49 offset:768
	s_waitcnt vmcnt(3)
	ds_write_b32 v141, v50
	ds_write_b32 v142, v51 offset:256
	ds_write_b32 v143, v52 offset:512
	ds_write_b32 v144, v53 offset:768
	s_waitcnt vmcnt(2)
	ds_write_b32 v145, v54
	ds_write_b32 v146, v55 offset:256
	ds_write_b32 v147, v56 offset:512
	ds_write_b32 v148, v57 offset:768
	s_waitcnt vmcnt(1)
	ds_write_b32 v149, v58
	ds_write_b32 v150, v59 offset:256
	ds_write_b32 v151, v60 offset:512
	ds_write_b32 v152, v61 offset:768
	s_waitcnt vmcnt(0)
	ds_write_b32 v153, v62
	ds_write_b32 v154, v63 offset:256
	ds_write_b32 v155, v64 offset:512
	ds_write_b32 v156, v65 offset:768
	s_waitcnt lgkmcnt(0)
	s_add_i32 s63, s63, 1
	s_cmp_lg_u32 s63, 2
	s_cbranch_scc1 .LBB0_684
	v_mov_b32_e32 v0, 0
	s_and_saveexec_b64 s[2:3], s[4:5]
	s_cbranch_execz .LBB0_683
	s_mov_b64 s[18:19], exec
	v_mbcnt_lo_u32_b32 v0, s18, 0
	v_mbcnt_hi_u32_b32 v0, s19, v0
	v_cmp_eq_u32_e32 vcc, 0, v0
	s_and_saveexec_b64 s[16:17], vcc
	s_cbranch_execz .LBB0_682
	s_bcnt1_i32_b64 s0, s[18:19]
	s_lshl_b32 s0, s0, 1
	v_mov_b32_e32 v66, s0
	global_atomic_add v66, v1, v66, s[12:13] sc0
